# finish phase: next row's loads overlap this row's math (wait moved to the copies at the loop end); attention K/V prefetch rotated through two register sets
# baseline (speedup 1.0000x reference)
.LBB0_626:
	s_or_b64 exec, exec, s[30:31]
	v_readlane_b32 s0, v255, 32
	v_readlane_b32 s1, v255, 33
	s_cmp_eq_u32 s0, 3
	s_cselect_b64 s[2:3], -1, 0
	s_cmp_lg_u32 s0, 3
	v_readlane_b32 s0, v252, 18
	v_writelane_b32 v255, s2, 37
	v_readlane_b32 s1, v252, 19
	s_cselect_b64 s[58:59], -1, 0
	v_writelane_b32 v255, s3, 38
	s_andn2_b64 vcc, exec, s[0:1]
	s_mov_b64 s[0:1], -1
	s_waitcnt lgkmcnt(0)
	s_barrier
	s_cbranch_vccnz .LBB0_676
	s_mov_b32 s101, 0
	v_readlane_b32 s0, v255, 37
	v_readlane_b32 s1, v255, 38
	s_and_b64 s[0:1], s[0:1], exec
	s_movk_i32 s0, 0x240
	s_cselect_b32 s16, 0x200, s0
	v_readlane_b32 s0, v252, 29
	s_cmp_lt_u32 s0, s16
	v_mov_b32_e32 v2, v0
	s_cbranch_scc0 .LBB0_672
	v_lshlrev_b32_e32 v3, 3, v2
	v_and_b32_e32 v4, 63, v2
	v_ashrrev_i32_e32 v159, 7, v2
	v_ashrrev_i32_e32 v156, 3, v2
	v_and_b32_e32 v158, 56, v3
	v_and_b32_e32 v3, 31, v2
	v_bfe_u32 v5, v2, 5, 1
	v_lshrrev_b32_e32 v2, 1, v2
	s_movk_i32 s0, 0x90
	v_cmp_gt_u32_e64 s[2:3], 32, v4
	v_mov_b32_e32 v4, 0x1200
	v_mov_b32_e32 v130, v131
	v_mov_b32_e32 v36, v131
	v_mov_b32_e32 v37, v131
	v_and_or_b32 v160, v2, 32, v3
	v_mul_lo_u32 v163, v156, s0
	v_lshlrev_b32_e32 v2, 2, v5
	v_mad_u32_u24 v176, v3, s0, v4
	s_movk_i32 s0, 0x88
	v_mov_b32_e32 v4, 0x1100
	v_mov_b32_e32 v132, v131
	v_mov_b32_e32 v133, v131
	v_mov_b32_e32 v34, v131
	v_mov_b32_e32 v35, v131
	v_mov_b64_e32 v[38:39], v[130:131]
	v_mov_b64_e32 v[68:69], v[36:37]
	v_mov_b64_e32 v[78:79], v[130:131]
	v_mov_b64_e32 v[92:93], v[36:37]
	v_mov_b64_e32 v[94:95], v[130:131]
	v_lshlrev_b32_e32 v162, 3, v5
	v_ashrrev_i32_e32 v157, 31, v156
	v_lshlrev_b32_e32 v161, 6, v159
	s_waitcnt vmcnt(0)
	v_lshlrev_b32_e32 v170, 4, v5
	v_or_b32_e32 v171, 0xffffff80, v2
	v_or_b32_e32 v172, 0xffffff80, v160
	v_or_b32_e32 v173, 0x80, v160
	v_mul_u32_u24_e32 v174, 0x88, v158
	v_mul_u32_u24_e32 v175, 0x90, v3
	v_mul_u32_u24_e32 v177, 0x88, v3
	v_mad_u32_u24 v178, v3, s0, v4
	s_mov_b64 s[6:7], -1
	v_lshlrev_b32_e32 v164, 1, v2
	v_mov_b64_e32 v[40:41], v[132:133]
	v_mov_b64_e32 v[66:67], v[34:35]
	v_mov_b64_e32 v[80:81], v[132:133]
	v_mov_b64_e32 v[90:91], v[34:35]
	v_mov_b64_e32 v[96:97], v[132:133]
	v_readlane_b32 s8, v252, 29
	s_branch .LBB0_631

.LBB0_661:
	s_andn2_b64 vcc, exec, s[12:13]
	s_cbranch_vccnz .Lattn_noload
	s_ashr_i32 s1, s0, 31
	v_lshl_add_u64 v[34:35], s[0:1], 0, v[156:157]
	v_readlane_b32 s0, v252, 30
	v_lshlrev_b64 v[36:37], 8, v[34:35]
	v_readlane_b32 s1, v252, 31
	v_mov_b64_e32 v[38:39], s[92:93]
	v_lshlrev_b32_e32 v130, 1, v158
	v_lshl_add_u64 v[36:37], s[0:1], 0, v[36:37]
	s_lshl_b64 s[0:1], s[14:15], 1
	s_movk_i32 s14, 0x3800
	v_mad_u64_u32 v[38:39], s[12:13], v34, s14, v[38:39]
	v_mad_i32_i24 v39, v35, s14, v39
	v_lshl_add_u64 v[34:35], v[38:39], 0, s[0:1]
	v_lshl_add_u64 v[36:37], v[36:37], 0, s[0:1]
	v_lshl_add_u64 v[34:35], v[34:35], 0, v[130:131]
	v_lshl_add_u64 v[36:37], v[36:37], 0, v[130:131]
	v_add_co_u32_e32 v34, vcc, 0x6cdc000, v34
	s_movk_i32 s81, 0x3800
	s_nop 0
	v_addc_co_u32_e32 v35, vcc, 0, v35, vcc
	s_bitcmp1_b32 s101, 0
	s_cbranch_scc1 .Lattn_ld_odd
	global_load_dwordx4 v[118:121], v[36:37], off
	global_load_dwordx4 v[114:117], v[34:35], off offset:2848
	s_branch .LBB0_663
.Lattn_ld_odd:
	global_load_dwordx4 v[90:93], v[36:37], off
	global_load_dwordx4 v[94:97], v[34:35], off offset:2848
	s_branch .LBB0_663
.Lattn_noload:
	s_waitcnt vmcnt(0)
.LBB0_663:
	v_add3_u32 v46, s30, v175, v170
	v_add3_u32 v50, s30, v176, v170
	ds_read_b128 v[34:37], v46
	ds_read_b128 v[38:41], v46 offset:32
	ds_read_b128 v[42:45], v46 offset:64
	ds_read_b128 v[46:49], v46 offset:96
	ds_read_b128 v[180:183], v50
	ds_read_b128 v[184:187], v50 offset:32
	ds_read_b128 v[188:191], v50 offset:64
	ds_read_b128 v[198:201], v50 offset:96
	v_add3_u32 v50, s30, v177, v162
	v_add3_u32 v51, s30, v178, v162
	v_add_u32_e32 v50, 0x2000, v50
	v_add_u32_e32 v51, 0x2000, v51
	ds_read2_b64 v[152:155], v50 offset0:128 offset1:130
	ds_read2_b64 v[144:147], v50 offset0:132 offset1:134
	ds_read2_b64 v[148:151], v51 offset0:128 offset1:130
	ds_read2_b64 v[140:143], v51 offset0:132 offset1:134
	ds_read2_b64 v[136:139], v50 offset0:136 offset1:138
	ds_read2_b64 v[132:135], v51 offset0:136 offset1:138
	ds_read2_b64 v[126:129], v50 offset0:140 offset1:142
	ds_read2_b64 v[122:125], v51 offset0:140 offset1:142
	v_mov_b32 v50, 0
	s_nop 0
	v_mov_b32_e32 v51, v50
	v_mov_b32_e32 v52, v50
	v_mov_b32_e32 v53, v50
	v_mov_b32_e32 v54, v50
	v_mov_b32_e32 v55, v50
	v_mov_b32_e32 v56, v50
	v_mov_b32_e32 v57, v50
	v_mov_b32_e32 v58, v50
	v_mov_b32_e32 v59, v50
	v_mov_b32_e32 v60, v50
	v_mov_b32_e32 v61, v50
	v_mov_b32_e32 v62, v50
	v_mov_b32_e32 v63, v50
	v_mov_b32_e32 v64, v50
	v_mov_b32_e32 v65, v50
	s_waitcnt lgkmcnt(14)
	s_nop 0
	v_mfma_f32_32x32x16_bf16 v[50:65], v[34:37], v[98:101], v[50:65]
	v_mov_b32 v34, 0
	s_nop 0
	v_mov_b32_e32 v35, v34
	v_mov_b32_e32 v36, v34
	v_mov_b32_e32 v37, v34
	v_mfma_f32_32x32x16_bf16 v[50:65], v[38:41], v[102:105], v[50:65]
	v_mov_b32_e32 v38, v34
	v_mov_b32_e32 v39, v34
	v_mov_b32_e32 v40, v34
	v_mov_b32_e32 v41, v34
	s_waitcnt lgkmcnt(13)
	v_mfma_f32_32x32x16_bf16 v[50:65], v[42:45], v[106:109], v[50:65]
	v_mov_b32_e32 v42, v34
	v_mov_b32_e32 v43, v34
	v_mov_b32_e32 v44, v34
	v_mov_b32_e32 v45, v34
	s_waitcnt lgkmcnt(12)
	v_mfma_f32_32x32x16_bf16 v[50:65], v[46:49], v[110:113], v[50:65]
	v_mov_b32_e32 v46, v34
	v_mov_b32_e32 v47, v34
	v_mov_b32_e32 v48, v34
	v_mov_b32_e32 v49, v34
	s_waitcnt lgkmcnt(11)
	s_nop 0
	v_mfma_f32_32x32x16_bf16 v[34:49], v[180:183], v[98:101], v[34:49]
	s_waitcnt lgkmcnt(10)
	v_mfma_f32_32x32x16_bf16 v[34:49], v[184:187], v[102:105], v[34:49]
	s_waitcnt lgkmcnt(9)
	v_mfma_f32_32x32x16_bf16 v[34:49], v[188:191], v[106:109], v[34:49]
	s_waitcnt lgkmcnt(8)
	v_mfma_f32_32x32x16_bf16 v[34:49], v[198:201], v[110:113], v[34:49]
	s_cmp_gt_i32 s28, s20
	s_cbranch_scc1 .LBB0_670
	s_add_i32 s14, s28, s19
	s_cmp_lt_i32 s14, 4
	s_cbranch_scc1 .LBB0_666
	s_cmp_eq_u32 s14, 4
	s_cselect_b64 s[0:1], -1, 0
	s_cbranch_execz .LBB0_667
	s_branch .LBB0_668

.LBB0_670:
	v_max_f32_e32 v130, v51, v51
	v_max_f32_e32 v180, v50, v50
	v_max_f32_e32 v130, v180, v130
	v_max3_f32 v130, v130, v52, v53
	v_max3_f32 v130, v130, v54, v55
	v_max3_f32 v130, v130, v56, v57
	v_max3_f32 v130, v130, v58, v59
	v_max3_f32 v130, v130, v60, v61
	v_max3_f32 v130, v130, v62, v63
	v_max3_f32 v130, v130, v64, v65
	v_max3_f32 v130, v130, v34, v35
	v_max3_f32 v130, v130, v36, v37
	v_max3_f32 v130, v130, v38, v39
	v_max3_f32 v130, v130, v40, v41
	v_max3_f32 v130, v130, v42, v43
	v_max3_f32 v130, v130, v44, v45
	v_max3_f32 v130, v130, v46, v47
	v_max3_f32 v130, v130, v48, v49
	v_mov_b32_e32 v180, v130
	v_mov_b32_e32 v181, v130
	s_nop 1
	v_permlane32_swap_b32_e32 v180, v181
	v_cndmask_b32_e64 v180, v180, v181, s[2:3]
	v_max3_f32 v130, v179, v130, v180
	v_sub_f32_e32 v50, v50, v130
	v_exp_f32_e32 v50, v50
	v_sub_f32_e32 v51, v51, v130
	v_exp_f32_e32 v51, v51
	v_sub_f32_e32 v52, v52, v130
	v_exp_f32_e32 v52, v52
	v_sub_f32_e32 v53, v53, v130
	v_exp_f32_e32 v53, v53
	v_sub_f32_e32 v54, v54, v130
	v_add_f32_e32 v180, 0, v50
	v_exp_f32_e32 v54, v54
	v_sub_f32_e32 v55, v55, v130
	v_add_f32_e32 v180, v51, v180
	v_exp_f32_e32 v55, v55
	v_sub_f32_e32 v56, v56, v130
	v_add_f32_e32 v180, v52, v180
	v_exp_f32_e32 v56, v56
	v_sub_f32_e32 v57, v57, v130
	v_add_f32_e32 v180, v53, v180
	v_exp_f32_e32 v57, v57
	v_sub_f32_e32 v58, v58, v130
	v_add_f32_e32 v180, v54, v180
	v_exp_f32_e32 v58, v58
	v_sub_f32_e32 v59, v59, v130
	v_add_f32_e32 v180, v55, v180
	v_exp_f32_e32 v59, v59
	v_sub_f32_e32 v60, v60, v130
	v_add_f32_e32 v180, v56, v180
	v_exp_f32_e32 v60, v60
	v_sub_f32_e32 v61, v61, v130
	v_add_f32_e32 v180, v57, v180
	v_exp_f32_e32 v61, v61
	v_sub_f32_e32 v62, v62, v130
	v_add_f32_e32 v180, v58, v180
	v_exp_f32_e32 v62, v62
	v_sub_f32_e32 v63, v63, v130
	v_add_f32_e32 v180, v59, v180
	v_exp_f32_e32 v63, v63
	v_sub_f32_e32 v64, v64, v130
	v_add_f32_e32 v180, v60, v180
	v_exp_f32_e32 v64, v64
	v_sub_f32_e32 v65, v65, v130
	v_add_f32_e32 v180, v61, v180
	v_exp_f32_e32 v65, v65
	v_sub_f32_e32 v34, v34, v130
	v_add_f32_e32 v180, v62, v180
	v_exp_f32_e32 v181, v34
	v_sub_f32_e32 v34, v35, v130
	v_add_f32_e32 v180, v63, v180
	v_exp_f32_e32 v182, v34
	v_sub_f32_e32 v35, v36, v130
	v_add_f32_e32 v34, v64, v180
	v_exp_f32_e32 v180, v35
	v_sub_f32_e32 v35, v37, v130
	v_add_f32_e32 v34, v65, v34
	v_exp_f32_e32 v183, v35
	v_sub_f32_e32 v35, v38, v130
	v_add_f32_e32 v34, v181, v34
	v_exp_f32_e32 v184, v35
	v_sub_f32_e32 v35, v39, v130
	v_add_f32_e32 v34, v182, v34
	v_exp_f32_e32 v39, v35
	v_add_f32_e32 v34, v180, v34
	v_sub_f32_e32 v179, v179, v130
	v_add_f32_e32 v34, v183, v34
	v_add_f32_e32 v34, v184, v34
	v_exp_f32_e32 v38, v179
	v_add_f32_e32 v185, v39, v34
	v_sub_f32_e32 v34, v40, v130
	v_exp_f32_e32 v40, v34
	v_sub_f32_e32 v34, v41, v130
	v_exp_f32_e32 v41, v34
	v_sub_f32_e32 v34, v42, v130
	v_exp_f32_e32 v42, v34
	v_pk_mul_f32 v[32:33], v[32:33], v[38:39] op_sel_hi:[1,0]
	v_pk_mul_f32 v[30:31], v[30:31], v[38:39] op_sel_hi:[1,0]
	v_pk_mul_f32 v[28:29], v[28:29], v[38:39] op_sel_hi:[1,0]
	v_pk_mul_f32 v[26:27], v[26:27], v[38:39] op_sel_hi:[1,0]
	v_pk_mul_f32 v[24:25], v[24:25], v[38:39] op_sel_hi:[1,0]
	v_pk_mul_f32 v[22:23], v[22:23], v[38:39] op_sel_hi:[1,0]
	v_pk_mul_f32 v[20:21], v[20:21], v[38:39] op_sel_hi:[1,0]
	v_pk_mul_f32 v[18:19], v[18:19], v[38:39] op_sel_hi:[1,0]
	v_pk_mul_f32 v[16:17], v[16:17], v[38:39] op_sel_hi:[1,0]
	v_cvt_pk_bf16_f32 v34, v50, v51
	v_cvt_pk_bf16_f32 v35, v52, v53
	v_cvt_pk_bf16_f32 v36, v54, v55
	v_cvt_pk_bf16_f32 v37, v56, v57
	v_pk_mul_f32 v[14:15], v[14:15], v[38:39] op_sel_hi:[1,0]
	v_pk_mul_f32 v[12:13], v[12:13], v[38:39] op_sel_hi:[1,0]
	v_pk_mul_f32 v[10:11], v[10:11], v[38:39] op_sel_hi:[1,0]
	v_pk_mul_f32 v[8:9], v[8:9], v[38:39] op_sel_hi:[1,0]
	v_pk_mul_f32 v[6:7], v[6:7], v[38:39] op_sel_hi:[1,0]
	v_pk_mul_f32 v[4:5], v[4:5], v[38:39] op_sel_hi:[1,0]
	v_pk_mul_f32 v[2:3], v[2:3], v[38:39] op_sel_hi:[1,0]
	s_waitcnt lgkmcnt(7)
	v_mfma_f32_32x32x16_bf16 v[18:33], v[152:155], v[34:37], v[18:33]
	v_sub_f32_e32 v43, v43, v130
	v_exp_f32_e32 v43, v43
	v_sub_f32_e32 v44, v44, v130
	v_exp_f32_e32 v44, v44
	v_sub_f32_e32 v45, v45, v130
	v_exp_f32_e32 v45, v45
	v_sub_f32_e32 v46, v46, v130
	s_waitcnt lgkmcnt(5)
	v_mfma_f32_32x32x16_bf16 v[2:17], v[148:151], v[34:37], v[2:17]
	v_add_f32_e32 v34, v40, v185
	v_add_f32_e32 v34, v41, v34
	v_add_f32_e32 v50, v42, v34
	v_cvt_pk_bf16_f32 v34, v58, v59
	v_cvt_pk_bf16_f32 v35, v60, v61
	v_cvt_pk_bf16_f32 v36, v62, v63
	v_cvt_pk_bf16_f32 v37, v64, v65
	v_add_f32_e32 v50, v43, v50
	s_add_i32 s28, s28, 1
	v_mfma_f32_32x32x16_bf16 v[18:33], v[144:147], v[34:37], v[18:33]
	s_cmp_ge_i32 s28, s26
	s_waitcnt lgkmcnt(4)
	v_mfma_f32_32x32x16_bf16 v[2:17], v[140:143], v[34:37], v[2:17]
	v_add_f32_e32 v34, v44, v50
	v_add_f32_e32 v50, v45, v34
	v_cvt_pk_bf16_f32 v34, v181, v182
	v_cvt_pk_bf16_f32 v35, v180, v183
	v_cvt_pk_bf16_f32 v36, v184, v39
	v_cvt_pk_bf16_f32 v37, v40, v41
	v_exp_f32_e32 v39, v46
	v_sub_f32_e32 v40, v47, v130
	s_waitcnt lgkmcnt(3)
	v_mfma_f32_32x32x16_bf16 v[18:33], v[136:139], v[34:37], v[18:33]
	v_exp_f32_e32 v40, v40
	v_sub_f32_e32 v41, v48, v130
	v_exp_f32_e32 v41, v41
	v_add_f32_e32 v46, v39, v50
	v_add_f32_e32 v46, v40, v46
	v_add_f32_e32 v46, v41, v46
	s_waitcnt lgkmcnt(2)
	v_mfma_f32_32x32x16_bf16 v[2:17], v[132:135], v[34:37], v[2:17]
	v_sub_f32_e32 v34, v49, v130
	v_exp_f32_e32 v47, v34
	v_cvt_pk_bf16_f32 v34, v42, v43
	v_cvt_pk_bf16_f32 v35, v44, v45
	v_cvt_pk_bf16_f32 v36, v39, v40
	v_cvt_pk_bf16_f32 v37, v41, v47
	v_add_f32_e32 v39, v47, v46
	v_mov_b32_e32 v40, v39
	s_waitcnt lgkmcnt(1)
	v_mfma_f32_32x32x16_bf16 v[18:33], v[126:129], v[34:37], v[18:33]
	v_mov_b32_e32 v41, v39
	s_nop 1
	v_permlane32_swap_b32_e32 v40, v41
	v_cndmask_b32_e64 v40, v40, v41, s[2:3]
	v_add_f32_e32 v42, v39, v40
	v_fmac_f32_e32 v42, v165, v38
	v_mov_b64_e32 v[38:39], v[78:79]
	s_waitcnt lgkmcnt(0)
	v_mfma_f32_32x32x16_bf16 v[2:17], v[122:125], v[34:37], v[2:17]
	v_mov_b64_e32 v[34:35], v[66:67]
	v_mov_b64_e32 v[36:37], v[68:69]
	v_mov_b64_e32 v[40:41], v[80:81]
	s_waitcnt vmcnt(2)
	s_bitcmp1_b32 s101, 0
	s_cbranch_scc1 .Lattn_rot_odd
	v_mov_b64_e32 v[66:67], v[90:91]
	v_mov_b64_e32 v[78:79], v[94:95]
	v_mov_b64_e32 v[68:69], v[92:93]
	v_mov_b64_e32 v[80:81], v[96:97]
	s_branch .Lattn_rot_join
.Lattn_rot_odd:
	v_mov_b64_e32 v[66:67], v[118:119]
	v_mov_b64_e32 v[78:79], v[114:115]
	v_mov_b64_e32 v[68:69], v[120:121]
	v_mov_b64_e32 v[80:81], v[116:117]
.Lattn_rot_join:
	s_xor_b32 s101, s101, 1
	s_cmp_ge_i32 s28, s26
	s_cbranch_scc1 .LBB0_630
	v_mov_b32_e32 v179, v130
	v_mov_b32_e32 v165, v42
	s_branch .LBB0_651

.LBB0_819:
	s_or_b64 exec, exec, s[0:1]
	v_lshlrev_b32_e32 v102, 16, v86
	v_and_b32_e32 v103, 0xffff0000, v86
	v_lshlrev_b32_e32 v86, 16, v87
	v_and_b32_e32 v87, 0xffff0000, v87
	v_lshlrev_b32_e32 v104, 16, v82
	v_and_b32_e32 v105, 0xffff0000, v82
	v_lshlrev_b32_e32 v82, 16, v83
	v_and_b32_e32 v83, 0xffff0000, v83
	v_pk_add_f32 v[82:83], v[82:83], v[86:87]
	v_pk_add_f32 v[86:87], v[104:105], v[102:103]
	v_lshlrev_b32_e32 v102, 16, v88
	v_mul_f32_e32 v106, v87, v87
	v_and_b32_e32 v103, 0xffff0000, v88
	v_lshlrev_b32_e32 v104, 16, v84
	v_and_b32_e32 v105, 0xffff0000, v84
	v_fmac_f32_e32 v106, v86, v86
	v_pk_add_f32 v[102:103], v[104:105], v[102:103]
	v_fmac_f32_e32 v106, v82, v82
	v_lshlrev_b32_e32 v88, 16, v89
	v_and_b32_e32 v89, 0xffff0000, v89
	v_lshlrev_b32_e32 v84, 16, v85
	v_and_b32_e32 v85, 0xffff0000, v85
	v_fmac_f32_e32 v106, v83, v83
	v_pk_mul_f32 v[104:105], v[102:103], v[102:103]
	v_pk_add_f32 v[84:85], v[84:85], v[88:89]
	v_add_f32_e32 v104, v104, v106
	v_pk_mul_f32 v[88:89], v[84:85], v[84:85]
	v_add_f32_e32 v104, v105, v104
	v_add_f32_e32 v88, v88, v104
	v_add_f32_e32 v88, v89, v88
	s_movk_i32 s3, 0xc00
	s_add_i32 s2, s2, 1
	v_add_f32_dpp v88, v88, v88 row_ror:8 row_mask:0xf bank_mask:0xf bound_ctrl:1
	s_movk_i32 s44, 0xc00
	s_cmp_lg_u32 s2, 9
	v_add_f32_dpp v88, v88, v88 row_half_mirror row_mask:0xf bank_mask:0xf bound_ctrl:1
	s_nop 1
	v_add_f32_dpp v88, v88, v88 quad_perm:[1,0,3,2] row_mask:0xf bank_mask:0xf bound_ctrl:1
	s_nop 1
	v_add_f32_dpp v88, v88, v88 quad_perm:[2,3,0,1] row_mask:0xf bank_mask:0xf bound_ctrl:1
	v_fmamk_f32 v88, v88, 0x3c000000, v1
	v_rsq_f32_e32 v88, v88
	s_nop 0
	v_pk_mul_f32 v[102:103], v[102:103], v[88:89] op_sel_hi:[1,0]
	v_pk_mul_f32 v[86:87], v[86:87], v[88:89] op_sel_hi:[1,0]
	v_pk_mul_f32 v[82:83], v[82:83], v[88:89] op_sel_hi:[1,0]
	v_pk_mul_f32 v[84:85], v[84:85], v[88:89] op_sel_hi:[1,0]
	v_pk_mul_f32 v[88:89], v[2:3], v[102:103]
	v_lshlrev_b32_e32 v102, 16, v78
	v_and_b32_e32 v103, 0xffff0000, v78
	v_mul_f32_e32 v78, 0xbfb8aa3b, v102
	v_exp_f32_e32 v78, v78
	v_pk_mul_f32 v[86:87], v[6:7], v[86:87]
	v_pk_mul_f32 v[82:83], v[8:9], v[82:83]
	v_pk_mul_f32 v[84:85], v[4:5], v[84:85]
	v_add_f32_e32 v78, 1.0, v78
	v_rcp_f32_e32 v104, v78
	v_mul_f32_e32 v78, 0xbfb8aa3b, v103
	v_exp_f32_e32 v78, v78
	s_nop 0
	v_add_f32_e32 v78, 1.0, v78
	v_rcp_f32_e32 v105, v78
	s_nop 0
	v_pk_mul_f32 v[102:103], v[104:105], v[102:103]
	s_nop 0
	v_pk_mul_f32 v[86:87], v[102:103], v[86:87]
	v_lshlrev_b32_e32 v102, 16, v80
	v_mul_f32_e32 v78, 0xbfb8aa3b, v102
	v_exp_f32_e32 v78, v78
	v_and_b32_e32 v103, 0xffff0000, v80
	v_add_f32_e32 v78, 1.0, v78
	v_rcp_f32_e32 v104, v78
	v_mul_f32_e32 v78, 0xbfb8aa3b, v103
	v_exp_f32_e32 v78, v78
	s_nop 0
	v_add_f32_e32 v78, 1.0, v78
	v_rcp_f32_e32 v105, v78
	v_lshlrev_b32_e32 v78, 16, v79
	v_mul_f32_e32 v80, 0xbfb8aa3b, v78
	v_exp_f32_e32 v80, v80
	v_pk_mul_f32 v[102:103], v[104:105], v[102:103]
	v_and_b32_e32 v79, 0xffff0000, v79
	v_pk_mul_f32 v[88:89], v[102:103], v[88:89]
	v_add_f32_e32 v80, 1.0, v80
	v_rcp_f32_e32 v102, v80
	v_mul_f32_e32 v80, 0xbfb8aa3b, v79
	v_exp_f32_e32 v80, v80
	s_nop 0
	v_add_f32_e32 v80, 1.0, v80
	v_rcp_f32_e32 v103, v80
	s_nop 0
	v_pk_mul_f32 v[78:79], v[102:103], v[78:79]
	s_nop 0
	v_pk_mul_f32 v[82:83], v[78:79], v[82:83]
	v_lshlrev_b32_e32 v78, 16, v81
	v_and_b32_e32 v79, 0xffff0000, v81
	v_mul_f32_e32 v80, 0xbfb8aa3b, v78
	v_mul_f32_e32 v81, 0xbfb8aa3b, v79
	v_exp_f32_e32 v80, v80
	v_exp_f32_e32 v81, v81
	v_add_f32_e32 v80, 1.0, v80
	v_add_f32_e32 v81, 1.0, v81
	v_rcp_f32_e32 v80, v80
	v_rcp_f32_e32 v81, v81
	s_nop 0
	v_pk_mul_f32 v[78:79], v[80:81], v[78:79]
	s_nop 0
	v_pk_mul_f32 v[84:85], v[78:79], v[84:85]
	v_cvt_pk_bf16_f32 v78, v86, v87
	v_cvt_pk_bf16_f32 v79, v82, v83
	v_cvt_pk_bf16_f32 v80, v88, v89
	v_cvt_pk_bf16_f32 v81, v84, v85
	v_mad_i64_i32 v[82:83], s[0:1], v93, s3, v[98:99]
	global_store_dwordx4 v[82:83], v[78:81], off
	s_nop 1
	v_lshlrev_b32_e32 v79, 16, v59
	v_lshlrev_b32_e32 v78, 16, v58
	v_and_b32_e32 v59, 0xffff0000, v59
	v_and_b32_e32 v58, 0xffff0000, v58
	v_pk_fma_f32 v[58:59], v[10:11], v[58:59], v[78:79]
	v_lshlrev_b32_e32 v79, 16, v67
	v_lshlrev_b32_e32 v78, 16, v66
	v_and_b32_e32 v67, 0xffff0000, v67
	v_and_b32_e32 v66, 0xffff0000, v66
	v_pk_fma_f32 v[66:67], v[22:23], v[66:67], v[78:79]
	v_pk_add_f32 v[58:59], v[58:59], v[66:67]
	v_lshlrev_b32_e32 v66, 16, v18
	v_and_b32_e32 v67, 0xffff0000, v18
	v_mul_f32_e32 v18, 0x3d372713, v66
	v_mul_f32_e32 v18, v18, v66
	v_mov_b32_e32 v78, v66
	v_fmac_f32_e32 v78, v18, v78
	v_mul_f32_e32 v18, 0x3f4c422a, v78
	v_mul_f32_e32 v18, -2.0, v18
	v_mul_f32_e32 v18, 0x3fb8aa3b, v18
	v_exp_f32_e32 v18, v18
	v_mov_b32_e32 v79, v67
	v_add_f32_e32 v18, 1.0, v18
	v_rcp_f32_e32 v78, v18
	v_mul_f32_e32 v18, 0x3d372713, v67
	v_mul_f32_e32 v18, v18, v67
	v_fmac_f32_e32 v79, v18, v79
	v_mul_f32_e32 v18, 0x3f4c422a, v79
	v_mul_f32_e32 v18, -2.0, v18
	v_mul_f32_e32 v18, 0x3fb8aa3b, v18
	v_exp_f32_e32 v18, v18
	s_nop 0
	v_add_f32_e32 v18, 1.0, v18
	v_rcp_f32_e32 v79, v18
	s_nop 0
	v_pk_mul_f32 v[66:67], v[78:79], v[66:67]
	s_nop 0
	v_pk_mul_f32 v[58:59], v[66:67], v[58:59]
	v_lshlrev_b32_e32 v67, 16, v31
	v_lshlrev_b32_e32 v66, 16, v30
	v_and_b32_e32 v31, 0xffff0000, v31
	v_and_b32_e32 v30, 0xffff0000, v30
	v_pk_fma_f32 v[30:31], v[14:15], v[30:31], v[66:67]
	v_lshlrev_b32_e32 v67, 16, v35
	v_lshlrev_b32_e32 v66, 16, v34
	v_and_b32_e32 v35, 0xffff0000, v35
	v_and_b32_e32 v34, 0xffff0000, v34
	v_pk_fma_f32 v[34:35], v[26:27], v[34:35], v[66:67]
	v_pk_add_f32 v[30:31], v[30:31], v[34:35]
	v_lshlrev_b32_e32 v34, 16, v20
	v_mul_f32_e32 v18, 0x3d372713, v34
	v_and_b32_e32 v35, 0xffff0000, v20
	v_mul_f32_e32 v18, v18, v34
	v_mov_b32_e32 v20, v34
	v_fmac_f32_e32 v20, v18, v20
	v_mul_f32_e32 v18, 0x3f4c422a, v20
	v_mul_f32_e32 v18, -2.0, v18
	v_mul_f32_e32 v18, 0x3fb8aa3b, v18
	v_exp_f32_e32 v18, v18
	v_mov_b32_e32 v20, v35
	v_add_f32_e32 v18, 1.0, v18
	v_rcp_f32_e32 v66, v18
	v_mul_f32_e32 v18, 0x3d372713, v35
	v_mul_f32_e32 v18, v18, v35
	v_fmac_f32_e32 v20, v18, v20
	v_mul_f32_e32 v18, 0x3f4c422a, v20
	v_mul_f32_e32 v18, -2.0, v18
	v_mul_f32_e32 v18, 0x3fb8aa3b, v18
	v_exp_f32_e32 v18, v18
	s_nop 0
	v_add_f32_e32 v18, 1.0, v18
	v_rcp_f32_e32 v67, v18
	v_lshlrev_b32_e32 v18, 16, v19
	v_mul_f32_e32 v20, 0x3d372713, v18
	v_mul_f32_e32 v20, v20, v18
	v_pk_mul_f32 v[34:35], v[66:67], v[34:35]
	v_and_b32_e32 v67, 0xffff0000, v69
	v_pk_mul_f32 v[30:31], v[34:35], v[30:31]
	v_lshlrev_b32_e32 v35, 16, v61
	v_lshlrev_b32_e32 v34, 16, v60
	v_and_b32_e32 v61, 0xffff0000, v61
	v_and_b32_e32 v60, 0xffff0000, v60
	v_pk_fma_f32 v[34:35], v[12:13], v[60:61], v[34:35]
	v_lshlrev_b32_e32 v61, 16, v69
	v_lshlrev_b32_e32 v60, 16, v68
	v_and_b32_e32 v66, 0xffff0000, v68
	v_pk_fma_f32 v[60:61], v[24:25], v[66:67], v[60:61]
	v_and_b32_e32 v19, 0xffff0000, v19
	v_pk_add_f32 v[34:35], v[34:35], v[60:61]
	v_mov_b32_e32 v60, v18
	v_fmac_f32_e32 v60, v20, v60
	v_mul_f32_e32 v20, 0x3f4c422a, v60
	v_mul_f32_e32 v20, -2.0, v20
	v_mul_f32_e32 v20, 0x3fb8aa3b, v20
	v_exp_f32_e32 v20, v20
	v_mov_b32_e32 v61, v19
	v_add_f32_e32 v20, 1.0, v20
	v_rcp_f32_e32 v60, v20
	v_mul_f32_e32 v20, 0x3d372713, v19
	v_mul_f32_e32 v20, v20, v19
	v_fmac_f32_e32 v61, v20, v61
	v_mul_f32_e32 v20, 0x3f4c422a, v61
	v_mul_f32_e32 v20, -2.0, v20
	v_mul_f32_e32 v20, 0x3fb8aa3b, v20
	v_exp_f32_e32 v20, v20
	s_nop 0
	v_add_f32_e32 v20, 1.0, v20
	v_rcp_f32_e32 v61, v20
	v_lshlrev_b32_e32 v20, 16, v21
	v_and_b32_e32 v21, 0xffff0000, v21
	v_pk_mul_f32 v[18:19], v[60:61], v[18:19]
	s_nop 0
	v_pk_mul_f32 v[34:35], v[18:19], v[34:35]
	v_lshlrev_b32_e32 v19, 16, v33
	v_lshlrev_b32_e32 v18, 16, v32
	v_and_b32_e32 v33, 0xffff0000, v33
	v_and_b32_e32 v32, 0xffff0000, v32
	v_pk_fma_f32 v[18:19], v[16:17], v[32:33], v[18:19]
	v_lshlrev_b32_e32 v33, 16, v37
	v_lshlrev_b32_e32 v32, 16, v36
	v_and_b32_e32 v37, 0xffff0000, v37
	v_and_b32_e32 v36, 0xffff0000, v36
	v_pk_fma_f32 v[32:33], v[28:29], v[36:37], v[32:33]
	v_mov_b32_e32 v36, v21
	v_pk_add_f32 v[18:19], v[18:19], v[32:33]
	v_mul_f32_e32 v32, 0x3d372713, v20
	v_mul_f32_e32 v32, v32, v20
	v_mov_b32_e32 v33, v20
	v_fmac_f32_e32 v33, v32, v33
	v_mul_f32_e32 v32, 0x3f4c422a, v33
	v_mul_f32_e32 v33, 0x3d372713, v21
	v_mul_f32_e32 v33, v33, v21
	v_fmac_f32_e32 v36, v33, v36
	v_mul_f32_e32 v33, 0x3f4c422a, v36
	v_mul_f32_e32 v32, -2.0, v32
	v_mul_f32_e32 v33, -2.0, v33
	v_mul_f32_e32 v32, 0x3fb8aa3b, v32
	v_mul_f32_e32 v33, 0x3fb8aa3b, v33
	v_exp_f32_e32 v32, v32
	v_exp_f32_e32 v33, v33
	v_add_f32_e32 v32, 1.0, v32
	v_add_f32_e32 v33, 1.0, v33
	v_rcp_f32_e32 v32, v32
	v_rcp_f32_e32 v33, v33
	s_nop 0
	v_pk_mul_f32 v[20:21], v[32:33], v[20:21]
	s_nop 0
	v_pk_mul_f32 v[32:33], v[20:21], v[18:19]
	v_cvt_pk_bf16_f32 v20, v30, v31
	v_mov_b64_e32 v[30:31], s[92:93]
	v_mad_i64_i32 v[30:31], s[0:1], v93, s3, v[30:31]
	v_lshl_add_u64 v[30:31], v[30:31], 0, v[130:131]
	v_add_co_u32_e32 v30, vcc, 0x320be000, v30
	v_cvt_pk_bf16_f32 v18, v58, v59
	v_cvt_pk_bf16_f32 v19, v34, v35
	v_cvt_pk_bf16_f32 v21, v32, v33
	v_addc_co_u32_e32 v31, vcc, 0, v31, vcc
	global_store_dwordx4 v[30:31], v[18:21], off offset:768
	s_waitcnt vmcnt(2)
	v_mov_b64_e32 v[84:85], v[44:45]
	v_mov_b64_e32 v[88:89], v[40:41]
	v_mov_b64_e32 v[82:83], v[42:43]
	v_mov_b64_e32 v[86:87], v[38:39]
	v_mov_b64_e32 v[80:81], v[48:49]
	v_mov_b64_e32 v[78:79], v[46:47]
	v_mov_b64_e32 v[66:67], v[70:71]
	v_mov_b64_e32 v[68:69], v[72:73]
	v_mov_b64_e32 v[34:35], v[74:75]
	v_mov_b64_e32 v[30:31], v[62:63]
	v_mov_b64_e32 v[60:61], v[56:57]
	v_mov_b64_e32 v[18:19], v[50:51]
	v_mov_b64_e32 v[36:37], v[76:77]
	v_mov_b64_e32 v[32:33], v[64:65]
	v_mov_b64_e32 v[58:59], v[54:55]
	v_mov_b64_e32 v[20:21], v[52:53]
	s_cbranch_scc0 .LBB0_826
.LBB0_820:
	v_add_u32_e32 v93, s2, v90
	s_movk_i32 s0, 0x3fff
	v_cmp_lt_i32_e32 vcc, s0, v93
	s_and_saveexec_b64 s[0:1], vcc
	s_xor_b64 s[0:1], exec, s[0:1]
	v_add_u32_e32 v38, 0xffffc000, v93
	v_lshrrev_b32_e32 v38, 6, v38
	v_add_u32_e32 v102, 0x100, v38
	s_andn2_saveexec_b64 s[0:1], s[0:1]
	v_ashrrev_i32_e32 v38, 31, v93
	v_lshrrev_b32_e32 v38, 26, v38
	v_add_u32_e32 v38, v93, v38
	v_ashrrev_i32_e32 v102, 6, v38
	s_or_b64 exec, exec, s[0:1]
	s_cmp_lg_u32 s2, 8
	s_cselect_b64 vcc, -1, 0
	v_addc_co_u32_e32 v54, vcc, 0, v93, vcc
	v_ashrrev_i32_e32 v55, 31, v54
	v_lshlrev_b64 v[38:39], 10, v[54:55]
	v_lshl_add_u64 v[38:39], v[96:97], 0, v[38:39]
	v_mov_b64_e32 v[46:47], s[92:93]
	v_add_co_u32_e32 v42, vcc, 0x1200000, v38
	v_mad_i64_i32 v[46:47], s[0:1], v54, s81, v[46:47]
	s_nop 0
	v_addc_co_u32_e32 v43, vcc, 0, v39, vcc
	v_lshl_add_u64 v[46:47], v[46:47], 0, v[130:131]
	s_mov_b32 s0, 0x6cdc000
	v_add_co_u32_e32 v48, vcc, s0, v46
	s_mov_b32 s0, 0x6cdd000
	s_nop 0
	v_addc_co_u32_e32 v49, vcc, 0, v47, vcc
	v_lshlrev_b64 v[70:71], 9, v[54:55]
	v_add_co_u32_e32 v50, vcc, s0, v46
	v_or_b32_e32 v54, v70, v92
	v_mov_b32_e32 v55, v71
	v_readlane_b32 s0, v252, 23
	v_lshlrev_b64 v[54:55], 2, v[54:55]
	v_readlane_b32 s1, v252, 24
	v_addc_co_u32_e32 v51, vcc, 0, v47, vcc
	s_nop 0
	v_lshl_add_u64 v[56:57], s[0:1], 0, v[54:55]
	v_lshl_add_u64 v[54:55], s[92:93], 0, v[54:55]
	v_lshl_add_u64 v[70:71], v[70:71], 0, v[94:95]
	v_add_co_u32_e32 v62, vcc, s6, v54
	v_lshlrev_b64 v[70:71], 2, v[70:71]
	s_nop 0
	v_addc_co_u32_e32 v63, vcc, 0, v55, vcc
	v_lshl_add_u64 v[72:73], s[0:1], 0, v[70:71]
	v_lshl_add_u64 v[70:71], s[92:93], 0, v[70:71]
	v_add_co_u32_e32 v74, vcc, 0x28d5d000, v70
	global_load_dwordx4 v[38:41], v[38:39], off
	s_nop 0
	global_load_dwordx4 v[42:45], v[42:43], off
	v_addc_co_u32_e32 v75, vcc, 0, v71, vcc
	global_load_dwordx4 v[46:49], v[48:49], off offset:512
	s_nop 0
	global_load_dwordx4 v[50:53], v[50:51], off offset:32
	s_nop 0
	global_load_dwordx4 v[54:57], v[56:57], off
	s_nop 0
	global_load_dwordx4 v[62:65], v[62:63], off offset:2832
	s_nop 0
	global_load_dwordx4 v[70:73], v[72:73], off
	s_nop 0
	global_load_dwordx4 v[74:77], v[74:75], off offset:2832
	v_cmp_ne_u32_e32 vcc, v102, v91
	s_and_saveexec_b64 s[0:1], vcc
	s_cbranch_execz .LBB0_819
	v_ashrrev_i32_e32 v103, 31, v102
	v_lshlrev_b64 v[10:11], 11, v[102:103]
	v_lshl_add_u64 v[22:23], v[100:101], 0, v[10:11]
	s_mov_b64 s[4:5], 0x90000
	global_load_dwordx4 v[14:17], v[22:23], off offset:16
	global_load_dwordx4 v[10:13], v[22:23], off
	v_lshl_add_u64 v[26:27], v[22:23], 0, s[4:5]
	v_add_co_u32_e32 v22, vcc, 0x90000, v22
	v_mov_b32_e32 v91, v102
	s_nop 0
	v_addc_co_u32_e32 v23, vcc, 0, v23, vcc
	global_load_dwordx4 v[22:25], v[22:23], off
	s_nop 0
	global_load_dwordx4 v[26:29], v[26:27], off offset:16
	s_waitcnt vmcnt(0)
	s_branch .LBB0_819
